# barrier-wait conversion: waves stop taking new items only once 6 of the 8 XCCs have arrived (was: half of them), on top of best
# speedup vs baseline: 1.0037x; 1.0037x over previous
; __device__ __forceinline__ unsigned xb_ld(unsigned* p)              { return __hip_atomic_load(p, __ATOMIC_RELAXED, __HIP_MEMORY_SCOPE_AGENT); }
;     ...
;     for (;;) {
;         unsigned f = 0u; if (lane < 16) f = xb_ld(&bar[XB_FLAG(lane)]);
;         const bool waiting = (lane < 16) && ((mask >> lane) & 1u) && ((int)(f - gen) <= 0);
;         const unsigned long long wm = __builtin_amdgcn_ballot_w64(waiting);
;         if (wm == 0ull) break;
;         if (stopw && 2 * __builtin_popcountll(wm) <= __builtin_popcount(mask)) { *stopw = stopv; stopw = nullptr; }
;         __builtin_amdgcn_s_sleep(1);
;         if ((++sp & 255u) == 0u) { if (xb_ld(&bar[XB_TMO])) break; if (sp > XB_SPIN_CAP) { if (lane == 0) atomicAdd(&bar[XB_TMO], 1u); break; } }
;     }
.LBB0_244:
	s_or_b64 exec, exec, s[14:15]
	v_cndmask_b32_e64 v5, 0, 1, s[16:17]
	v_cmp_ne_u32_e32 vcc, 0, v5
	s_or_b64 s[12:13], s[12:13], exec
	s_cbranch_vccz .LBB0_252
	s_cmp_eq_u32 s18, 0
	s_mov_b32 s24, 0
	s_cbranch_scc1 .LBB0_249
	s_bcnt1_i32_b64 s14, vcc
	s_nop 0
	v_cmp_gt_u32_e64 vcc, s14, 2
	s_cbranch_vccnz .LBB0_248
	v_mov_b32_e32 v5, s18
	s_mov_b32 s18, 0
	ds_write_b32 v5, v4
